# baseline (speedup 1.0000x reference)
_Z11attn_kernelPKDF16_S0_S0_PfPDF16_S1_:
	v_and_b32_e32 v65, 63, v0
	s_lshl_b32 s3, s2, 7
	s_lshr_b32 s4, s2, 2
	s_and_b32 s3, s3, 0x180
	s_and_b32 s4, s4, 0x3ffffffe
	s_add_i32 s3, s3, s4
	s_bfe_u32 s2, s2, 0x10002
	s_or_b32 s40, s3, s2
	s_mov_b32 s41, 0
	s_lshl_b64 s[2:3], s[40:41], 2
	s_getpc_b64 s[4:5]
	s_add_u32 s4, s4, g_tab@rel32@lo+4
	s_addc_u32 s5, s5, g_tab@rel32@hi+12
	s_add_u32 s42, s4, s2
	s_addc_u32 s43, s5, s3
	s_load_dword s12, s[42:43], 0x0
	s_load_dwordx4 s[4:7], s[0:1], 0x8
	s_load_dword s76, s[42:43], 0x1000
	s_load_dwordx2 s[80:81], s[0:1], 0x0
	s_load_dwordx4 s[84:87], s[0:1], 0x18
	s_load_dwordx2 s[88:89], s[0:1], 0x28
	v_lshlrev_b32_e32 v2, 4, v0
	s_movk_i32 s8, 0x70
	v_readfirstlane_b32 s3, v0
	s_waitcnt lgkmcnt(0)
	s_add_u32 s70, s4, 0x2000
	s_addc_u32 s71, s5, 0
	s_add_u32 s72, s6, 0x2000
	s_addc_u32 s73, s7, 0
	s_and_b32 s2, s12, 3
	s_lshl_b32 s10, s2, 19
	v_bitop3_b32 v10, v2, s8, v0 bitop3:0x48
	s_add_u32 s8, s6, s10
	s_addc_u32 s9, s7, 0
	s_lshr_b32 s13, s3, 6
	s_bfe_u32 s40, s12, 0x70007
	s_bfe_u32 s33, s12, 0x6000e
	v_and_b32_e32 v1, 0x1f80, v2
	s_add_u32 s10, s4, s10
	v_or_b32_e32 v50, v10, v1
	v_mov_b32_e32 v51, 0
	s_addc_u32 s11, s5, 0
	v_lshl_add_u64 v[52:53], s[10:11], 0, v[50:51]
	v_lshl_add_u64 v[54:55], s[8:9], 0, v[50:51]
	s_lshl_b32 s8, s40, 13
	s_mov_b32 s9, s41
	s_lshl_b32 s50, s13, 10
	v_lshl_add_u64 v[2:3], v[52:53], 0, s[8:9]
	s_mov_b32 m0, s50
	s_add_i32 s51, s50, 0x2000
	global_load_lds_dwordx4 v[2:3], off
	v_lshl_add_u64 v[2:3], v[54:55], 0, s[8:9]
	s_mov_b32 m0, s51
	s_cmp_eq_u32 s33, 0
	global_load_lds_dwordx4 v[2:3], off
	s_cbranch_scc1 .LBB2_30
	s_mov_b64 s[14:15], s[80:81]
	s_mov_b64 s[8:9], s[84:85]
	s_mov_b64 s[10:11], s[86:87]
	s_mov_b64 s[44:45], s[88:89]
	s_cmp_lt_u32 s13, 4
	s_cbranch_scc1 .Lattn_prio_done
	s_setprio 1
.Lattn_prio_done:
	s_lshl_b32 s52, s13, 4
	s_lshl_b32 s0, s2, 12
	v_and_b32_e32 v56, 15, v0
	v_bfe_u32 v15, v0, 4, 2
	v_lshrrev_b32_e32 v14, 1, v0
	v_bfe_u32 v2, v0, 1, 3
	s_add_i32 s54, s52, s0
	v_lshlrev_b32_e32 v16, 7, v56
	v_bitop3_b32 v3, v15, v14, 7 bitop3:0x78
	v_bitop3_b32 v2, v15, v2, 4 bitop3:0x36
	s_bfe_u32 s53, s12, 0x50002
	v_or_b32_e32 v18, s54, v56
	v_lshl_or_b32 v57, v3, 4, v16
	v_lshl_or_b32 v81, v2, 4, v16
	v_lshl_add_u32 v2, s53, 7, v18
	v_mov_b32_e32 v3, v51
	v_lshlrev_b64 v[2:3], 7, v[2:3]
	v_and_b32_e32 v50, 48, v0
	s_waitcnt lgkmcnt(0)
	v_lshl_add_u64 v[2:3], s[14:15], 0, v[2:3]
	v_lshl_add_u64 v[12:13], v[2:3], 0, v[50:51]
	global_load_dwordx4 v[2:5], v[12:13], off offset:64
	global_load_dwordx4 v[6:9], v[12:13], off
	v_and_b32_e32 v11, 63, v0
	v_bfe_u32 v12, v0, 5, 1
	s_mulk_i32 s13, 0xc00
	v_and_b32_e32 v13, 7, v0
	v_cmp_gt_u32_e64 s[0:1], 16, v11
	v_bitop3_b32 v11, v12, v0, 7 bitop3:0x78
	s_lshr_b32 s55, s3, 8
	s_add_i32 s3, s50, s13
	v_and_b32_e32 v14, 8, v14
	v_lshlrev_b32_e32 v23, 4, v11
	v_bitop3_b32 v11, v12, v13, 2 bitop3:0x36
	v_add3_u32 v19, s3, v16, v14
	v_bfe_u32 v14, v0, 3, 3
	v_lshlrev_b32_e32 v24, 4, v11
	v_bitop3_b32 v11, v12, v13, 4 bitop3:0x36
	v_bitop3_b32 v16, v14, v0, 7 bitop3:0x78
	v_lshlrev_b32_e32 v25, 4, v11
	v_bitop3_b32 v11, v12, v13, 6 bitop3:0x36
	v_bitop3_b32 v0, v15, v0, 15 bitop3:0x78
	v_lshl_add_u64 v[58:59], s[14:15], 0, v[50:51]
	v_lshlrev_b32_e32 v50, 4, v13
	v_lshlrev_b32_e32 v13, 4, v11
	v_or_b32_e32 v11, 8, v14
	v_lshlrev_b32_e32 v86, 4, v0
	v_bitop3_b32 v0, v15, v56, 4 bitop3:0x36
	v_or_b32_e32 v17, 4, v15
	v_lshl_add_u32 v21, v16, 4, s3
	v_lshlrev_b32_e32 v26, 7, v14
	v_lshlrev_b32_e32 v12, 6, v14
	v_lshlrev_b32_e32 v27, 7, v11
	v_lshlrev_b32_e32 v14, 6, v11
	v_lshlrev_b32_e32 v87, 4, v0
	v_or_b32_e32 v0, 8, v15
	v_bitop3_b32 v11, v15, v56, 8 bitop3:0x36
	v_bitop3_b32 v16, v15, v56, 12 bitop3:0x36
	v_lshlrev_b32_e32 v83, 2, v15
	v_add_u32_e32 v84, 0x80, v18
	v_lshl_add_u64 v[60:61], s[10:11], 0, v[50:51]
	v_lshlrev_b32_e32 v50, 4, v56
	v_lshlrev_b32_e32 v88, 4, v11
	v_or_b32_e32 v11, 12, v15
	v_lshlrev_b32_e32 v89, 4, v16
	v_lshl_add_u32 v28, v15, 8, s3
	v_lshlrev_b32_e32 v16, 6, v15
	v_lshl_add_u32 v15, v17, 8, s3
	v_lshlrev_b32_e32 v18, 6, v17
	v_lshl_add_u32 v17, v0, 8, s3
	v_lshlrev_b32_e32 v20, 6, v0
	v_add_u32_e32 v0, v1, v10
	v_lshl_add_u64 v[62:63], s[8:9], 0, v[50:51]
	s_lshl_b32 s8, s53, 1
	v_lshl_or_b32 v50, s2, 19, v0
	s_mov_b64 s[46:47], 0x2000
	v_lshl_add_u32 v85, v56, 8, s3
	v_lshl_add_u32 v29, v11, 8, s3
	v_lshlrev_b32_e32 v22, 6, v11
	s_add_i32 s3, s55, s8
	v_lshl_add_u64 v[10:11], v[50:51], 0, s[46:47]
	v_or_b32_e32 v82, s52, v56
	s_add_i32 s56, s8, 2
	s_sub_i32 s57, 0, s3
	v_lshl_add_u64 v[0:1], s[4:5], 0, v[10:11]
	s_and_b32 s78, s50, 0xc00
	s_lshl_b32 s78, s78, 1
	v_lshrrev_b32_e32 v77, 3, v65
	v_lshrrev_b32_e32 v78, 4, v65
	v_and_b32_e32 v79, 7, v65
	v_xor_b32_e32 v78, v79, v78
	v_lshlrev_b32_e32 v78, 4, v78
	v_lshl_add_u32 v77, v77, 7, v78
	v_add_u32_e32 v77, s78, v77
	v_lshl_or_b32 v64, s2, 19, v77
	v_add_u32_e32 v65, 0x400, v64
	v_xor_b32_e32 v65, 64, v65
	s_mov_b32 s58, 0x40c00000
	s_mov_b32 s36, 0x3c003c00
	v_mov_b32_e32 v116, s36
	v_mov_b32_e32 v117, s36
	v_mov_b32_e32 v118, s36
	v_mov_b32_e32 v119, s36
	v_add_u32_e32 v90, v19, v23
	v_add_u32_e32 v91, v19, v24
	v_add_u32_e32 v92, v19, v25
	v_add_u32_e32 v93, v19, v13
	v_add_u32_e32 v94, v21, v26
	v_lshlrev_b32_e32 v50, 1, v12
	v_add_u32_e32 v95, v21, v27
	v_lshlrev_b32_e32 v66, 1, v14
	v_add_u32_e32 v96, v28, v86
	v_lshlrev_b32_e32 v68, 2, v16
	v_add_u32_e32 v97, v15, v87
	v_lshlrev_b32_e32 v70, 2, v18
	v_add_u32_e32 v98, v17, v88
	v_lshlrev_b32_e32 v72, 2, v20
	v_add_u32_e32 v99, v29, v89
	v_lshlrev_b32_e32 v74, 2, v22
	v_mov_b32_e32 v100, 0xff800000
	v_mov_b32_e32 v101, 0xf149f2ca
	s_mov_b32 s59, s41
	s_branch .LBB2_3

.LBB2_3:
	s_lshl_b32 s63, s53, 1
	s_add_i32 s61, s63, 2
	s_sub_i32 s2, s61, s40
	s_lshl_b32 s60, s53, 7
	s_min_i32 s62, s33, s2
	s_cmp_eq_u32 s55, 0
	s_cselect_b32 s79, 0, s62
	s_cmp_lt_i32 s2, 1
	s_waitcnt vmcnt(0)
	s_barrier
	s_cbranch_scc1 .LBB2_21
	s_add_i32 s63, s63, s55
	v_lshl_or_b32 v11, s63, 6, v83
	v_add_u32_e32 v10, s60, v82
	v_or_b32_e32 v12, 2, v11
	v_cmp_gt_i32_e64 s[6:7], v12, v10
	v_or_b32_e32 v12, 3, v11
	v_cmp_gt_i32_e64 s[8:9], v12, v10
	v_or_b32_e32 v12, 16, v11
	v_cmp_gt_i32_e64 s[10:11], v12, v10
	v_or_b32_e32 v12, 17, v11
	v_cmp_gt_i32_e64 s[12:13], v12, v10
	v_or_b32_e32 v12, 18, v11
	v_cmp_gt_i32_e64 s[14:15], v12, v10
	v_or_b32_e32 v12, 19, v11
	v_cmp_gt_i32_e64 s[16:17], v12, v10
	v_or_b32_e32 v12, 32, v11
	v_cmp_gt_i32_e64 s[18:19], v12, v10
	v_or_b32_e32 v12, 33, v11
	v_cmp_gt_i32_e64 s[20:21], v12, v10
	v_or_b32_e32 v12, 34, v11
	v_cmp_gt_i32_e64 s[22:23], v12, v10
	v_or_b32_e32 v12, 35, v11
	v_cmp_gt_i32_e64 s[24:25], v12, v10
	v_or_b32_e32 v12, 48, v11
	s_sub_i32 s37, s56, s40
	v_cmp_gt_i32_e64 s[26:27], v12, v10
	v_or_b32_e32 v12, 49, v11
	s_min_i32 s37, s33, s37
	v_cmp_gt_i32_e64 s[2:3], v11, v10
	v_cmp_lt_i32_e64 s[4:5], v11, v10
	v_cmp_gt_i32_e64 s[28:29], v12, v10
	v_or_b32_e32 v12, 50, v11
	v_or_b32_e32 v11, 51, v11
	s_max_i32 s37, s37, 1
	s_lshl_b64 s[38:39], s[40:41], 13
	v_mov_b32_e32 v67, 0
	v_cmp_gt_i32_e64 s[30:31], v12, v10
	v_cmp_gt_i32_e64 s[34:35], v11, v10
	s_mov_b32 s64, 1
	s_sub_i32 s65, 0, s37
	s_add_i32 s66, s40, s57
	s_add_u32 s68, s70, s38
	s_addc_u32 s69, s71, s39
	s_add_u32 s74, s72, s38
	s_addc_u32 s75, s73, s39
	v_mov_b32_e32 v14, v51
	v_mov_b32_e32 v15, v51
	v_mov_b32_e32 v16, v51
	v_mov_b32_e32 v17, v51
	s_mov_b64 s[38:39], -1
	v_mov_b32_e32 v30, 0
	v_mov_b32_e32 v31, v67
	v_mov_b32_e32 v32, v67
	v_mov_b32_e32 v33, v67
	v_mov_b32_e32 v26, 0
	v_mov_b32_e32 v27, v67
	v_mov_b32_e32 v28, v67
	v_mov_b32_e32 v29, v67
	v_mov_b32_e32 v22, v67
	v_mov_b32_e32 v23, v67
	v_mov_b32_e32 v24, v67
	v_mov_b32_e32 v25, v67
	v_mov_b32_e32 v18, v67
	v_mov_b32_e32 v19, v67
	v_mov_b32_e32 v20, v67
	v_mov_b32_e32 v21, v67
	v_mov_b32_e32 v10, v67
	v_mov_b32_e32 v11, v67
	v_mov_b32_e32 v12, v67
	v_mov_b32_e32 v13, v67
	s_branch .LBB2_7

.LBB2_7:
	s_add_i32 s37, s64, -1
	s_and_b32 s37, s37, 1
	s_lshl_b32 s37, s37, 14
	s_add_i32 s48, s40, s64
	s_add_i32 s48, s48, -1
	s_cmp_gt_u32 s48, s63
	s_cbranch_scc1 .Lattn_skip_tile
	v_or_b32_e32 v114, s37, v57
	v_or_b32_e32 v115, s37, v81
	ds_read_b128 v[34:37], v114
	ds_read_b128 v[38:41], v114 offset:2048
	ds_read_b128 v[42:45], v114 offset:4096
	ds_read_b128 v[110:113], v115 offset:2048
	ds_read_b128 v[46:49], v114 offset:6144
	s_cmp_ge_i32 s64, s79
	s_cbranch_scc1 .Lattn_no_dma
	s_xor_b32 s48, s37, 0x4000
	s_add_i32 s48, s78, s48
	s_mov_b32 m0, s48
	s_nop 0
	global_load_lds_dwordx4 v64, s[68:69]
	s_add_i32 m0, s48, 0x400
	s_nop 0
	global_load_lds_dwordx4 v65, s[68:69]
	s_add_i32 m0, s48, 0x2000
	s_nop 0
	global_load_lds_dwordx4 v64, s[74:75]
	s_add_i32 m0, s48, 0x2400
	s_nop 0
	global_load_lds_dwordx4 v65, s[74:75]

.Lattn_skip_tile:
	s_branch .LBB2_6
